# stack: indexer scoring loops (f32 relu+fmac, ping-pong acc) + hgrn prefix loads in flight + exp1 next-unit loads under one wait + combine 22 loads in flight per row; alignment-preserving pads
# speedup vs baseline: 1.0093x; 1.0093x over previous
.LBB0_3486:
	s_xor_b64 s[16:17], s[24:25], -1
	s_and_b64 vcc, exec, s[16:17]
	v_mov_b32_e32 v194, v168
	v_mov_b32_e32 v195, v170
	v_mov_b32_e32 v196, v172
	v_mov_b32_e32 v197, v174
	s_cbranch_vccnz .LBB0_3488
	s_lshl_b32 s15, s87, 8
	v_add_u32_e32 v194, s15, v188
	v_lshlrev_b32_e32 v194, 2, v194
	global_load_dword v194, v194, s[8:9]
	v_add_u32_e32 v195, s15, v190
	v_lshlrev_b32_e32 v195, 2, v195
	global_load_dword v195, v195, s[8:9]
	s_bitset1_b32 s15, 7
	v_add_u32_e32 v196, s15, v188
	v_lshlrev_b32_e32 v196, 2, v196
	global_load_dword v196, v196, s[8:9]
	v_add_u32_e32 v197, s15, v190
	v_lshlrev_b32_e32 v197, 2, v197
	global_load_dword v197, v197, s[8:9]
	s_waitcnt vmcnt(0)
	v_readfirstlane_b32 s14, v2
	v_lshl_add_u32 v194, v194, 11, v189
	v_lshl_add_u32 v195, v195, 11, v191
	v_lshl_add_u32 v196, v196, 11, v189
	v_lshl_add_u32 v197, v197, 11, v191
	s_nop 0
	s_nop 0
	s_nop 0
	s_nop 0
	s_nop 0
	s_nop 0
	s_nop 0
	s_nop 0
	s_nop 0
	s_nop 0
	s_nop 0
	s_nop 0

.LBB0_3777:
	v_ashrrev_i32_e32 v11, 31, v10
	v_lshlrev_b64 v[6:7], 14, v[10:11]
	v_mov_b32_e32 v11, v54
	v_mov_b32_e32 v12, 0
	v_lshlrev_b32_e32 v2, 4, v11
	v_add_u32_e32 v8, 0x400, v2
	v_ashrrev_i32_e32 v3, 31, v2
	v_ashrrev_i32_e32 v9, 31, v8
	v_lshl_add_u64 v[4:5], v[6:7], 0, v[2:3]
	v_lshl_add_u64 v[6:7], v[6:7], 0, v[8:9]
	v_lshl_add_u64 v[4:5], s[46:47], 0, v[4:5]
	v_lshl_add_u64 v[6:7], s[46:47], 0, v[6:7]
	s_mov_b64 s[8:9], 0
	v_mov_b32_e32 v13, v12
	v_mov_b32_e32 v38, v12
	v_mov_b32_e32 v39, v12
	v_mov_b32_e32 v40, v12
	v_mov_b32_e32 v41, v12
	v_mov_b32_e32 v34, v12
	v_mov_b32_e32 v35, v12
	v_mov_b32_e32 v36, v12
	v_mov_b32_e32 v37, v12
	v_mov_b32_e32 v30, v12
	v_mov_b32_e32 v31, v12
	v_mov_b32_e32 v32, v12
	v_mov_b32_e32 v33, v12
	v_mov_b32_e32 v26, v12
	v_mov_b32_e32 v27, v12
	v_mov_b32_e32 v28, v12
	v_mov_b32_e32 v29, v12
	v_mov_b32_e32 v22, v12
	v_mov_b32_e32 v23, v12
	v_mov_b32_e32 v24, v12
	v_mov_b32_e32 v25, v12
	v_mov_b32_e32 v8, v12
	v_mov_b32_e32 v9, v12
	v_mov_b32_e32 v20, v12
	v_mov_b32_e32 v21, v12
	v_mov_b32_e32 v16, v12
	v_mov_b32_e32 v17, v12
	v_mov_b32_e32 v18, v12
	v_mov_b32_e32 v19, v12
	v_mov_b32_e32 v14, v12
	v_mov_b32_e32 v15, v12
	s_mov_b32 s13, 0
	s_mov_b32 s12, 0x14138c00
	v_lshl_add_u64 v[68:69], v[4:5], 0, s[12:13]
	s_mov_b32 s12, 0x14139c00
	v_lshl_add_u64 v[70:71], v[4:5], 0, s[12:13]
	s_mov_b32 s12, 0x1413ac00
	v_lshl_add_u64 v[72:73], v[4:5], 0, s[12:13]
	s_mov_b32 s12, 0x1413bc00
	v_lshl_add_u64 v[74:75], v[4:5], 0, s[12:13]
	global_load_dwordx4 v[96:99], v[68:69], off
	global_load_dwordx4 v[100:103], v[68:69], off offset:1024
	global_load_dwordx4 v[104:107], v[68:69], off offset:2048
	global_load_dwordx4 v[108:111], v[68:69], off offset:3072
	global_load_dwordx4 v[112:115], v[70:71], off
	global_load_dwordx4 v[116:119], v[70:71], off offset:1024
	global_load_dwordx4 v[120:123], v[70:71], off offset:2048
	global_load_dwordx4 v[124:127], v[70:71], off offset:3072
	global_load_dwordx4 v[128:131], v[72:73], off
	global_load_dwordx4 v[132:135], v[72:73], off offset:1024
	global_load_dwordx4 v[136:139], v[72:73], off offset:2048
	global_load_dwordx4 v[140:143], v[72:73], off offset:3072
	global_load_dwordx4 v[144:147], v[74:75], off
	global_load_dwordx4 v[148:151], v[74:75], off offset:1024
	global_load_dwordx4 v[152:155], v[74:75], off offset:2048
	global_load_dwordx4 v[156:159], v[74:75], off offset:3072
	v_add_u32_e32 v180, s5, v10
	v_ashrrev_i32_e32 v181, 31, v180
	v_lshlrev_b64 v[180:181], 12, v[180:181]
	v_lshl_add_u64 v[180:181], s[62:63], 0, v[180:181]
	v_and_b32_e32 v182, 0xffffff00, v2
	v_lshrrev_b32_e32 v183, 1, v2
	s_movk_i32 s12, 0x60
	v_and_or_b32 v182, v183, s12, v182
	v_lshlrev_b32_e32 v183, 3, v11
	v_and_b32_e32 v183, 24, v183
	v_or_b32_e32 v182, v182, v183
	v_ashrrev_i32_e32 v183, 31, v182
	v_lshl_add_u64 v[180:181], v[182:183], 1, v[180:181]
	global_load_dwordx2 v[164:165], v[180:181], off
	global_load_dwordx2 v[166:167], v[180:181], off offset:8
	global_load_dwordx4 v[168:171], v[180:181], off offset:256
	global_load_dwordx2 v[172:173], v[180:181], off offset:2048
	global_load_dwordx2 v[174:175], v[180:181], off offset:2056
	global_load_dwordx4 v[176:179], v[180:181], off offset:2304
	s_waitcnt vmcnt(21)
	v_cvt_pk_f32_fp8_e32 v[76:77], v96
	v_cvt_pk_f32_fp8_sdwa v[78:79], v96 src0_sel:WORD_1
	v_cvt_pk_f32_fp8_e32 v[80:81], v97
	v_cvt_pk_f32_fp8_sdwa v[82:83], v97 src0_sel:WORD_1
	v_cvt_pk_f32_fp8_e32 v[84:85], v98
	v_cvt_pk_f32_fp8_sdwa v[86:87], v98 src0_sel:WORD_1
	v_cvt_pk_f32_fp8_e32 v[88:89], v99
	v_cvt_pk_f32_fp8_sdwa v[90:91], v99 src0_sel:WORD_1
	v_pk_add_f32 v[38:39], v[38:39], v[76:77]
	v_pk_add_f32 v[40:41], v[40:41], v[78:79]
	v_pk_add_f32 v[34:35], v[34:35], v[80:81]
	v_pk_add_f32 v[36:37], v[36:37], v[82:83]
	v_pk_add_f32 v[30:31], v[30:31], v[84:85]
	v_pk_add_f32 v[32:33], v[32:33], v[86:87]
	v_pk_add_f32 v[26:27], v[26:27], v[88:89]
	v_pk_add_f32 v[28:29], v[28:29], v[90:91]
	s_waitcnt vmcnt(20)
	v_cvt_pk_f32_fp8_e32 v[76:77], v100
	v_cvt_pk_f32_fp8_sdwa v[78:79], v100 src0_sel:WORD_1
	v_cvt_pk_f32_fp8_e32 v[80:81], v101
	v_cvt_pk_f32_fp8_sdwa v[82:83], v101 src0_sel:WORD_1
	v_cvt_pk_f32_fp8_e32 v[84:85], v102
	v_cvt_pk_f32_fp8_sdwa v[86:87], v102 src0_sel:WORD_1
	v_cvt_pk_f32_fp8_e32 v[88:89], v103
	v_cvt_pk_f32_fp8_sdwa v[90:91], v103 src0_sel:WORD_1
	v_pk_add_f32 v[22:23], v[22:23], v[76:77]
	v_pk_add_f32 v[24:25], v[24:25], v[78:79]
	v_pk_add_f32 v[8:9], v[8:9], v[80:81]
	v_pk_add_f32 v[20:21], v[20:21], v[82:83]
	v_pk_add_f32 v[16:17], v[16:17], v[84:85]
	v_pk_add_f32 v[18:19], v[18:19], v[86:87]
	v_pk_add_f32 v[14:15], v[14:15], v[88:89]
	v_pk_add_f32 v[12:13], v[12:13], v[90:91]
	s_waitcnt vmcnt(19)
	v_cvt_pk_f32_fp8_e32 v[76:77], v104
	v_cvt_pk_f32_fp8_sdwa v[78:79], v104 src0_sel:WORD_1
	v_cvt_pk_f32_fp8_e32 v[80:81], v105
	v_cvt_pk_f32_fp8_sdwa v[82:83], v105 src0_sel:WORD_1
	v_cvt_pk_f32_fp8_e32 v[84:85], v106
	v_cvt_pk_f32_fp8_sdwa v[86:87], v106 src0_sel:WORD_1
	v_cvt_pk_f32_fp8_e32 v[88:89], v107
	v_cvt_pk_f32_fp8_sdwa v[90:91], v107 src0_sel:WORD_1
	v_pk_add_f32 v[38:39], v[38:39], v[76:77]
	v_pk_add_f32 v[40:41], v[40:41], v[78:79]
	v_pk_add_f32 v[34:35], v[34:35], v[80:81]
	v_pk_add_f32 v[36:37], v[36:37], v[82:83]
	v_pk_add_f32 v[30:31], v[30:31], v[84:85]
	v_pk_add_f32 v[32:33], v[32:33], v[86:87]
	v_pk_add_f32 v[26:27], v[26:27], v[88:89]
	v_pk_add_f32 v[28:29], v[28:29], v[90:91]
	s_waitcnt vmcnt(18)
	v_cvt_pk_f32_fp8_e32 v[76:77], v108
	v_cvt_pk_f32_fp8_sdwa v[78:79], v108 src0_sel:WORD_1
	v_cvt_pk_f32_fp8_e32 v[80:81], v109
	v_cvt_pk_f32_fp8_sdwa v[82:83], v109 src0_sel:WORD_1
	v_cvt_pk_f32_fp8_e32 v[84:85], v110
	v_cvt_pk_f32_fp8_sdwa v[86:87], v110 src0_sel:WORD_1
	v_cvt_pk_f32_fp8_e32 v[88:89], v111
	v_cvt_pk_f32_fp8_sdwa v[90:91], v111 src0_sel:WORD_1
	v_pk_add_f32 v[22:23], v[22:23], v[76:77]
	v_pk_add_f32 v[24:25], v[24:25], v[78:79]
	v_pk_add_f32 v[8:9], v[8:9], v[80:81]
	v_pk_add_f32 v[20:21], v[20:21], v[82:83]
	v_pk_add_f32 v[16:17], v[16:17], v[84:85]
	v_pk_add_f32 v[18:19], v[18:19], v[86:87]
	v_pk_add_f32 v[14:15], v[14:15], v[88:89]
	v_pk_add_f32 v[12:13], v[12:13], v[90:91]
	s_waitcnt vmcnt(17)
	v_cvt_pk_f32_fp8_e32 v[76:77], v112
	v_cvt_pk_f32_fp8_sdwa v[78:79], v112 src0_sel:WORD_1
	v_cvt_pk_f32_fp8_e32 v[80:81], v113
	v_cvt_pk_f32_fp8_sdwa v[82:83], v113 src0_sel:WORD_1
	v_cvt_pk_f32_fp8_e32 v[84:85], v114
	v_cvt_pk_f32_fp8_sdwa v[86:87], v114 src0_sel:WORD_1
	v_cvt_pk_f32_fp8_e32 v[88:89], v115
	v_cvt_pk_f32_fp8_sdwa v[90:91], v115 src0_sel:WORD_1
	v_pk_add_f32 v[38:39], v[38:39], v[76:77]
	v_pk_add_f32 v[40:41], v[40:41], v[78:79]
	v_pk_add_f32 v[34:35], v[34:35], v[80:81]
	v_pk_add_f32 v[36:37], v[36:37], v[82:83]
	v_pk_add_f32 v[30:31], v[30:31], v[84:85]
	v_pk_add_f32 v[32:33], v[32:33], v[86:87]
	v_pk_add_f32 v[26:27], v[26:27], v[88:89]
	v_pk_add_f32 v[28:29], v[28:29], v[90:91]
	s_waitcnt vmcnt(16)
	v_cvt_pk_f32_fp8_e32 v[76:77], v116
	v_cvt_pk_f32_fp8_sdwa v[78:79], v116 src0_sel:WORD_1
	v_cvt_pk_f32_fp8_e32 v[80:81], v117
	v_cvt_pk_f32_fp8_sdwa v[82:83], v117 src0_sel:WORD_1
	v_cvt_pk_f32_fp8_e32 v[84:85], v118
	v_cvt_pk_f32_fp8_sdwa v[86:87], v118 src0_sel:WORD_1
	v_cvt_pk_f32_fp8_e32 v[88:89], v119
	v_cvt_pk_f32_fp8_sdwa v[90:91], v119 src0_sel:WORD_1
	v_pk_add_f32 v[22:23], v[22:23], v[76:77]
	v_pk_add_f32 v[24:25], v[24:25], v[78:79]
	v_pk_add_f32 v[8:9], v[8:9], v[80:81]
	v_pk_add_f32 v[20:21], v[20:21], v[82:83]
	v_pk_add_f32 v[16:17], v[16:17], v[84:85]
	v_pk_add_f32 v[18:19], v[18:19], v[86:87]
	v_pk_add_f32 v[14:15], v[14:15], v[88:89]
	v_pk_add_f32 v[12:13], v[12:13], v[90:91]
	s_waitcnt vmcnt(15)
	v_cvt_pk_f32_fp8_e32 v[76:77], v120
	v_cvt_pk_f32_fp8_sdwa v[78:79], v120 src0_sel:WORD_1
	v_cvt_pk_f32_fp8_e32 v[80:81], v121
	v_cvt_pk_f32_fp8_sdwa v[82:83], v121 src0_sel:WORD_1
	v_cvt_pk_f32_fp8_e32 v[84:85], v122
	v_cvt_pk_f32_fp8_sdwa v[86:87], v122 src0_sel:WORD_1
	v_cvt_pk_f32_fp8_e32 v[88:89], v123
	v_cvt_pk_f32_fp8_sdwa v[90:91], v123 src0_sel:WORD_1
	v_pk_add_f32 v[38:39], v[38:39], v[76:77]
	v_pk_add_f32 v[40:41], v[40:41], v[78:79]
	v_pk_add_f32 v[34:35], v[34:35], v[80:81]
	v_pk_add_f32 v[36:37], v[36:37], v[82:83]
	v_pk_add_f32 v[30:31], v[30:31], v[84:85]
	v_pk_add_f32 v[32:33], v[32:33], v[86:87]
	v_pk_add_f32 v[26:27], v[26:27], v[88:89]
	v_pk_add_f32 v[28:29], v[28:29], v[90:91]
	s_waitcnt vmcnt(14)
	v_cvt_pk_f32_fp8_e32 v[76:77], v124
	v_cvt_pk_f32_fp8_sdwa v[78:79], v124 src0_sel:WORD_1
	v_cvt_pk_f32_fp8_e32 v[80:81], v125
	v_cvt_pk_f32_fp8_sdwa v[82:83], v125 src0_sel:WORD_1
	v_cvt_pk_f32_fp8_e32 v[84:85], v126
	v_cvt_pk_f32_fp8_sdwa v[86:87], v126 src0_sel:WORD_1
	v_cvt_pk_f32_fp8_e32 v[88:89], v127
	v_cvt_pk_f32_fp8_sdwa v[90:91], v127 src0_sel:WORD_1
	v_pk_add_f32 v[22:23], v[22:23], v[76:77]
	v_pk_add_f32 v[24:25], v[24:25], v[78:79]
	v_pk_add_f32 v[8:9], v[8:9], v[80:81]
	v_pk_add_f32 v[20:21], v[20:21], v[82:83]
	v_pk_add_f32 v[16:17], v[16:17], v[84:85]
	v_pk_add_f32 v[18:19], v[18:19], v[86:87]
	v_pk_add_f32 v[14:15], v[14:15], v[88:89]
	v_pk_add_f32 v[12:13], v[12:13], v[90:91]
	s_waitcnt vmcnt(13)
	v_cvt_pk_f32_fp8_e32 v[76:77], v128
	v_cvt_pk_f32_fp8_sdwa v[78:79], v128 src0_sel:WORD_1
	v_cvt_pk_f32_fp8_e32 v[80:81], v129
	v_cvt_pk_f32_fp8_sdwa v[82:83], v129 src0_sel:WORD_1
	v_cvt_pk_f32_fp8_e32 v[84:85], v130
	v_cvt_pk_f32_fp8_sdwa v[86:87], v130 src0_sel:WORD_1
	v_cvt_pk_f32_fp8_e32 v[88:89], v131
	v_cvt_pk_f32_fp8_sdwa v[90:91], v131 src0_sel:WORD_1
	v_pk_add_f32 v[38:39], v[38:39], v[76:77]
	v_pk_add_f32 v[40:41], v[40:41], v[78:79]
	v_pk_add_f32 v[34:35], v[34:35], v[80:81]
	v_pk_add_f32 v[36:37], v[36:37], v[82:83]
	v_pk_add_f32 v[30:31], v[30:31], v[84:85]
	v_pk_add_f32 v[32:33], v[32:33], v[86:87]
	v_pk_add_f32 v[26:27], v[26:27], v[88:89]
	v_pk_add_f32 v[28:29], v[28:29], v[90:91]
	s_waitcnt vmcnt(12)
	v_cvt_pk_f32_fp8_e32 v[76:77], v132
	v_cvt_pk_f32_fp8_sdwa v[78:79], v132 src0_sel:WORD_1
	v_cvt_pk_f32_fp8_e32 v[80:81], v133
	v_cvt_pk_f32_fp8_sdwa v[82:83], v133 src0_sel:WORD_1
	v_cvt_pk_f32_fp8_e32 v[84:85], v134
	v_cvt_pk_f32_fp8_sdwa v[86:87], v134 src0_sel:WORD_1
	v_cvt_pk_f32_fp8_e32 v[88:89], v135
	v_cvt_pk_f32_fp8_sdwa v[90:91], v135 src0_sel:WORD_1
	v_pk_add_f32 v[22:23], v[22:23], v[76:77]
	v_pk_add_f32 v[24:25], v[24:25], v[78:79]
	v_pk_add_f32 v[8:9], v[8:9], v[80:81]
	v_pk_add_f32 v[20:21], v[20:21], v[82:83]
	v_pk_add_f32 v[16:17], v[16:17], v[84:85]
	v_pk_add_f32 v[18:19], v[18:19], v[86:87]
	v_pk_add_f32 v[14:15], v[14:15], v[88:89]
	v_pk_add_f32 v[12:13], v[12:13], v[90:91]
	s_waitcnt vmcnt(11)
	v_cvt_pk_f32_fp8_e32 v[76:77], v136
	v_cvt_pk_f32_fp8_sdwa v[78:79], v136 src0_sel:WORD_1
	v_cvt_pk_f32_fp8_e32 v[80:81], v137
	v_cvt_pk_f32_fp8_sdwa v[82:83], v137 src0_sel:WORD_1
	v_cvt_pk_f32_fp8_e32 v[84:85], v138
	v_cvt_pk_f32_fp8_sdwa v[86:87], v138 src0_sel:WORD_1
	v_cvt_pk_f32_fp8_e32 v[88:89], v139
	v_cvt_pk_f32_fp8_sdwa v[90:91], v139 src0_sel:WORD_1
	v_pk_add_f32 v[38:39], v[38:39], v[76:77]
	v_pk_add_f32 v[40:41], v[40:41], v[78:79]
	v_pk_add_f32 v[34:35], v[34:35], v[80:81]
	v_pk_add_f32 v[36:37], v[36:37], v[82:83]
	v_pk_add_f32 v[30:31], v[30:31], v[84:85]
	v_pk_add_f32 v[32:33], v[32:33], v[86:87]
	v_pk_add_f32 v[26:27], v[26:27], v[88:89]
	v_pk_add_f32 v[28:29], v[28:29], v[90:91]
	s_waitcnt vmcnt(10)
	v_cvt_pk_f32_fp8_e32 v[76:77], v140
	v_cvt_pk_f32_fp8_sdwa v[78:79], v140 src0_sel:WORD_1
	v_cvt_pk_f32_fp8_e32 v[80:81], v141
	v_cvt_pk_f32_fp8_sdwa v[82:83], v141 src0_sel:WORD_1
	v_cvt_pk_f32_fp8_e32 v[84:85], v142
	v_cvt_pk_f32_fp8_sdwa v[86:87], v142 src0_sel:WORD_1
	v_cvt_pk_f32_fp8_e32 v[88:89], v143
	v_cvt_pk_f32_fp8_sdwa v[90:91], v143 src0_sel:WORD_1
	v_pk_add_f32 v[22:23], v[22:23], v[76:77]
	v_pk_add_f32 v[24:25], v[24:25], v[78:79]
	v_pk_add_f32 v[8:9], v[8:9], v[80:81]
	v_pk_add_f32 v[20:21], v[20:21], v[82:83]
	v_pk_add_f32 v[16:17], v[16:17], v[84:85]
	v_pk_add_f32 v[18:19], v[18:19], v[86:87]
	v_pk_add_f32 v[14:15], v[14:15], v[88:89]
	v_pk_add_f32 v[12:13], v[12:13], v[90:91]
	s_waitcnt vmcnt(9)
	v_cvt_pk_f32_fp8_e32 v[76:77], v144
	v_cvt_pk_f32_fp8_sdwa v[78:79], v144 src0_sel:WORD_1
	v_cvt_pk_f32_fp8_e32 v[80:81], v145
	v_cvt_pk_f32_fp8_sdwa v[82:83], v145 src0_sel:WORD_1
	v_cvt_pk_f32_fp8_e32 v[84:85], v146
	v_cvt_pk_f32_fp8_sdwa v[86:87], v146 src0_sel:WORD_1
	v_cvt_pk_f32_fp8_e32 v[88:89], v147
	v_cvt_pk_f32_fp8_sdwa v[90:91], v147 src0_sel:WORD_1
	v_pk_add_f32 v[38:39], v[38:39], v[76:77]
	v_pk_add_f32 v[40:41], v[40:41], v[78:79]
	v_pk_add_f32 v[34:35], v[34:35], v[80:81]
	v_pk_add_f32 v[36:37], v[36:37], v[82:83]
	v_pk_add_f32 v[30:31], v[30:31], v[84:85]
	v_pk_add_f32 v[32:33], v[32:33], v[86:87]
	v_pk_add_f32 v[26:27], v[26:27], v[88:89]
	v_pk_add_f32 v[28:29], v[28:29], v[90:91]
	s_waitcnt vmcnt(8)
	v_cvt_pk_f32_fp8_e32 v[76:77], v148
	v_cvt_pk_f32_fp8_sdwa v[78:79], v148 src0_sel:WORD_1
	v_cvt_pk_f32_fp8_e32 v[80:81], v149
	v_cvt_pk_f32_fp8_sdwa v[82:83], v149 src0_sel:WORD_1
	v_cvt_pk_f32_fp8_e32 v[84:85], v150
	v_cvt_pk_f32_fp8_sdwa v[86:87], v150 src0_sel:WORD_1
	v_cvt_pk_f32_fp8_e32 v[88:89], v151
	v_cvt_pk_f32_fp8_sdwa v[90:91], v151 src0_sel:WORD_1
	v_pk_add_f32 v[22:23], v[22:23], v[76:77]
	v_pk_add_f32 v[24:25], v[24:25], v[78:79]
	v_pk_add_f32 v[8:9], v[8:9], v[80:81]
	v_pk_add_f32 v[20:21], v[20:21], v[82:83]
	v_pk_add_f32 v[16:17], v[16:17], v[84:85]
	v_pk_add_f32 v[18:19], v[18:19], v[86:87]
	v_pk_add_f32 v[14:15], v[14:15], v[88:89]
	v_pk_add_f32 v[12:13], v[12:13], v[90:91]
	s_waitcnt vmcnt(7)
	v_cvt_pk_f32_fp8_e32 v[76:77], v152
	v_cvt_pk_f32_fp8_sdwa v[78:79], v152 src0_sel:WORD_1
	v_cvt_pk_f32_fp8_e32 v[80:81], v153
	v_cvt_pk_f32_fp8_sdwa v[82:83], v153 src0_sel:WORD_1
	v_cvt_pk_f32_fp8_e32 v[84:85], v154
	v_cvt_pk_f32_fp8_sdwa v[86:87], v154 src0_sel:WORD_1
	v_cvt_pk_f32_fp8_e32 v[88:89], v155
	v_cvt_pk_f32_fp8_sdwa v[90:91], v155 src0_sel:WORD_1
	v_pk_add_f32 v[38:39], v[38:39], v[76:77]
	v_pk_add_f32 v[40:41], v[40:41], v[78:79]
	v_pk_add_f32 v[34:35], v[34:35], v[80:81]
	v_pk_add_f32 v[36:37], v[36:37], v[82:83]
	v_pk_add_f32 v[30:31], v[30:31], v[84:85]
	v_pk_add_f32 v[32:33], v[32:33], v[86:87]
	v_pk_add_f32 v[26:27], v[26:27], v[88:89]
	v_pk_add_f32 v[28:29], v[28:29], v[90:91]
	s_waitcnt vmcnt(6)
	v_cvt_pk_f32_fp8_e32 v[76:77], v156
	v_cvt_pk_f32_fp8_sdwa v[78:79], v156 src0_sel:WORD_1
	v_cvt_pk_f32_fp8_e32 v[80:81], v157
	v_cvt_pk_f32_fp8_sdwa v[82:83], v157 src0_sel:WORD_1
	v_cvt_pk_f32_fp8_e32 v[84:85], v158
	v_cvt_pk_f32_fp8_sdwa v[86:87], v158 src0_sel:WORD_1
	v_cvt_pk_f32_fp8_e32 v[88:89], v159
	v_cvt_pk_f32_fp8_sdwa v[90:91], v159 src0_sel:WORD_1
	v_pk_add_f32 v[22:23], v[22:23], v[76:77]
	v_pk_add_f32 v[24:25], v[24:25], v[78:79]
	v_pk_add_f32 v[8:9], v[8:9], v[80:81]
	v_pk_add_f32 v[20:21], v[20:21], v[82:83]
	v_pk_add_f32 v[16:17], v[16:17], v[84:85]
	v_pk_add_f32 v[18:19], v[18:19], v[86:87]
	v_pk_add_f32 v[14:15], v[14:15], v[88:89]
	v_pk_add_f32 v[12:13], v[12:13], v[90:91]
	s_waitcnt vmcnt(0)
	v_and_b32_e32 v3, 0xffffe000, v10
	v_add_u32_e32 v57, 0, v3
	v_lshlrev_b32_e32 v3, 3, v11
	v_add_u32_e32 v46, s5, v10
	v_and_b32_e32 v11, 24, v3
	v_and_b32_e32 v3, 0xffffff00, v2
	v_lshrrev_b32_e32 v2, 1, v2
	s_movk_i32 s8, 0x60
	v_ashrrev_i32_e32 v47, 31, v46
	v_and_or_b32 v55, v2, s8, v3
	v_lshlrev_b64 v[4:5], 12, v[46:47]
	v_or_b32_e32 v42, v55, v11
	v_lshl_add_u64 v[4:5], s[62:63], 0, v[4:5]
	v_lshlrev_b32_e32 v56, 2, v42
	v_ashrrev_i32_e32 v43, 31, v42
	v_add_u32_e32 v62, v57, v56
	v_lshl_add_u64 v[2:3], v[42:43], 1, v[4:5]
	ds_read_b128 v[48:51], v62
	ds_read_b128 v[58:61], v62 offset:16
	v_mov_b32_e32 v2, v164
	v_mov_b32_e32 v3, v165
	v_readlane_b32 s12, v253, 2
	v_readlane_b32 s26, v253, 16
	v_readlane_b32 s27, v253, 17
	s_mov_b32 s8, 0x800000
	v_add_u32_e32 v10, s52, v10
	v_readlane_b32 s13, v253, 3
	v_readlane_b32 s14, v253, 4
	v_readlane_b32 s15, v253, 5
	v_readlane_b32 s16, v253, 6
	v_readlane_b32 s17, v253, 7
	v_readlane_b32 s18, v253, 8
	v_readlane_b32 s19, v253, 9
	v_readlane_b32 s20, v253, 10
	v_readlane_b32 s21, v253, 11
	v_readlane_b32 s22, v253, 12
	v_readlane_b32 s23, v253, 13
	v_readlane_b32 s24, v253, 14
	v_readlane_b32 s25, v253, 15
	v_lshlrev_b32_e32 v6, 16, v2
	v_and_b32_e32 v7, 0xffff0000, v2
	v_lshlrev_b32_e32 v2, 16, v3
	v_and_b32_e32 v3, 0xffff0000, v3
	s_waitcnt lgkmcnt(1)
	v_pk_fma_f32 v[40:41], v[40:41], v[50:51], v[2:3]
	v_pk_fma_f32 v[44:45], v[38:39], v[48:49], v[6:7]
	v_add_f32_e32 v3, v40, v41
	v_add_f32_e32 v2, v44, v45
	v_add_f32_e32 v2, v2, v3
	v_ashrrev_i32_e32 v39, 31, v55
	v_mov_b32_e32 v38, v42
	v_add_f32_e32 v50, 0, v2
	v_lshl_add_u64 v[2:3], v[38:39], 1, v[4:5]
	v_mov_b32_e32 v6, v166
	v_mov_b32_e32 v7, v167
	v_add_u32_e32 v55, 0x400, v55
	v_lshlrev_b32_e32 v48, 16, v6
	v_and_b32_e32 v49, 0xffff0000, v6
	v_lshlrev_b32_e32 v6, 16, v7
	v_and_b32_e32 v7, 0xffff0000, v7
	s_waitcnt lgkmcnt(0)
	v_pk_fma_f32 v[36:37], v[36:37], v[60:61], v[6:7]
	v_pk_fma_f32 v[34:35], v[34:35], v[58:59], v[48:49]
	v_mov_b32_e32 v58, v168
	v_mov_b32_e32 v59, v169
	v_mov_b32_e32 v60, v170
	v_mov_b32_e32 v61, v171
	v_add_f32_e32 v6, v34, v35
	v_add_f32_e32 v7, v36, v37
	v_add_f32_e32 v6, v6, v7
	v_add_f32_e32 v52, v50, v6
	ds_read_b128 v[48:51], v62 offset:512
	v_lshlrev_b32_e32 v2, 16, v58
	v_and_b32_e32 v3, 0xffff0000, v58
	v_lshlrev_b32_e32 v6, 16, v59
	v_and_b32_e32 v7, 0xffff0000, v59
	s_waitcnt lgkmcnt(0)
	v_pk_fma_f32 v[32:33], v[32:33], v[50:51], v[6:7]
	v_pk_fma_f32 v[30:31], v[30:31], v[48:49], v[2:3]
	v_add_f32_e32 v3, v32, v33
	v_add_f32_e32 v2, v30, v31
	v_add_f32_e32 v2, v2, v3
	v_add_f32_e32 v58, v52, v2
	ds_read_b128 v[50:53], v62 offset:528
	v_lshlrev_b32_e32 v2, 16, v60
	v_and_b32_e32 v3, 0xffff0000, v60
	v_lshlrev_b32_e32 v6, 16, v61
	v_and_b32_e32 v7, 0xffff0000, v61
	s_waitcnt lgkmcnt(0)
	v_pk_fma_f32 v[48:49], v[28:29], v[52:53], v[6:7]
	v_pk_fma_f32 v[28:29], v[26:27], v[50:51], v[2:3]
	v_add_f32_e32 v3, v48, v49
	v_add_f32_e32 v2, v28, v29
	v_or_b32_e32 v26, v55, v11
	v_add_f32_e32 v2, v2, v3
	v_ashrrev_i32_e32 v27, 31, v26
	v_add_f32_e32 v58, v58, v2
	v_lshl_add_u64 v[2:3], v[26:27], 1, v[4:5]
	v_mov_b32_e32 v2, v172
	v_mov_b32_e32 v3, v173
	ds_read_b128 v[50:53], v62 offset:4096
	v_or_b32_e32 v11, 16, v56
	v_lshlrev_b32_e32 v6, 16, v2
	v_and_b32_e32 v7, 0xffff0000, v2
	v_lshlrev_b32_e32 v2, 16, v3
	v_and_b32_e32 v3, 0xffff0000, v3
	s_waitcnt lgkmcnt(0)
	v_pk_fma_f32 v[52:53], v[24:25], v[52:53], v[2:3]
	v_pk_fma_f32 v[50:51], v[22:23], v[50:51], v[6:7]
	v_add_f32_e32 v3, v52, v53
	v_add_f32_e32 v2, v50, v51
	v_add_f32_e32 v2, v2, v3
	v_ashrrev_i32_e32 v23, 31, v55
	v_mov_b32_e32 v22, v26
	v_add_f32_e32 v62, v58, v2
	v_add_u32_e32 v2, v57, v11
	v_lshl_add_u64 v[6:7], v[22:23], 1, v[4:5]
	ds_read_b128 v[58:61], v2 offset:4096
	v_mov_b32_e32 v2, v174
	v_mov_b32_e32 v3, v175
	v_or_b32_e32 v55, 0x200, v56
	v_add_u32_e32 v11, 0, v11
	v_lshlrev_b32_e32 v4, 16, v2
	v_and_b32_e32 v5, 0xffff0000, v2
	v_lshlrev_b32_e32 v2, 16, v3
	v_and_b32_e32 v3, 0xffff0000, v3
	s_waitcnt lgkmcnt(0)
	v_pk_fma_f32 v[24:25], v[20:21], v[60:61], v[2:3]
	v_pk_fma_f32 v[20:21], v[8:9], v[58:59], v[4:5]
	v_mov_b32_e32 v6, v176
	v_mov_b32_e32 v7, v177
	v_mov_b32_e32 v8, v178
	v_mov_b32_e32 v9, v179
	v_add_f32_e32 v2, v20, v21
	v_add_f32_e32 v3, v24, v25
	v_add_f32_e32 v2, v2, v3
	v_add_f32_e32 v60, v62, v2
	v_add_u32_e32 v2, v57, v55
	ds_read_b128 v[2:5], v2 offset:4096
	v_lshlrev_b32_e32 v58, 16, v6
	v_and_b32_e32 v59, 0xffff0000, v6
	v_lshlrev_b32_e32 v6, 16, v7
	v_and_b32_e32 v7, 0xffff0000, v7
	s_waitcnt lgkmcnt(0)
	v_pk_fma_f32 v[4:5], v[18:19], v[4:5], v[6:7]
	v_pk_fma_f32 v[2:3], v[16:17], v[2:3], v[58:59]
	v_add_f32_e32 v7, v4, v5
	v_add_f32_e32 v6, v2, v3
	v_add_f32_e32 v6, v6, v7
	v_or_b32_e32 v16, 0x210, v56
	v_add_f32_e32 v17, v60, v6
	v_add_u32_e32 v6, v57, v16
	ds_read_b128 v[58:61], v6 offset:4096
	v_lshlrev_b32_e32 v18, 16, v8
	v_and_b32_e32 v19, 0xffff0000, v8
	v_lshlrev_b32_e32 v6, 16, v9
	v_and_b32_e32 v7, 0xffff0000, v9
	s_waitcnt lgkmcnt(0)
	v_pk_fma_f32 v[6:7], v[12:13], v[60:61], v[6:7]
	v_pk_fma_f32 v[8:9], v[14:15], v[58:59], v[18:19]
	v_add_f32_e32 v13, v6, v7
	v_add_f32_e32 v12, v8, v9
	v_add_f32_e32 v12, v12, v13
	v_add_f32_e32 v12, v17, v12
	s_nop 1
	v_add_f32_dpp v12, v12, v12 quad_perm:[1,0,3,2] row_mask:0xf bank_mask:0xf bound_ctrl:1
	s_nop 1
	v_add_f32_dpp v12, v12, v12 quad_perm:[2,3,0,1] row_mask:0xf bank_mask:0xf bound_ctrl:1
	s_nop 1
	v_add_f32_dpp v12, v12, v12 row_half_mirror row_mask:0xf bank_mask:0xf bound_ctrl:1
	s_nop 1
	v_add_f32_dpp v12, v12, v12 row_mirror row_mask:0xf bank_mask:0xf bound_ctrl:1
	v_mov_b32_e32 v13, v12
	s_nop 1
	v_permlane16_swap_b32_e32 v12, v13
	v_add_f32_e32 v12, v12, v13
	v_mov_b32_e32 v13, v12
	s_nop 1
	v_permlane32_swap_b32_e32 v12, v13
	v_add_f32_e32 v12, v12, v13
	v_fmac_f32_e32 v41, 0xba000000, v12
	v_fmac_f32_e32 v45, 0xba000000, v12
	v_fmamk_f32 v40, v12, 0xba000000, v40
	v_fmamk_f32 v44, v12, 0xba000000, v44
	v_mul_f32_e32 v13, v45, v45
	v_mul_f32_e32 v14, v41, v41
	v_fmac_f32_e32 v13, v44, v44
	v_fmac_f32_e32 v14, v40, v40
	v_fmac_f32_e32 v37, 0xba000000, v12
	v_fmac_f32_e32 v35, 0xba000000, v12
	v_add_f32_e32 v13, v13, v14
	v_fmamk_f32 v36, v12, 0xba000000, v36
	v_fmamk_f32 v34, v12, 0xba000000, v34
	v_mul_f32_e32 v14, v35, v35
	v_mul_f32_e32 v15, v37, v37
	v_fmac_f32_e32 v14, v34, v34
	v_fmac_f32_e32 v15, v36, v36
	v_add_f32_e32 v14, v14, v15
	v_fmac_f32_e32 v33, 0xba000000, v12
	v_fmac_f32_e32 v31, 0xba000000, v12
	v_add_f32_e32 v13, v13, v14
	v_fmamk_f32 v32, v12, 0xba000000, v32
	v_fmamk_f32 v30, v12, 0xba000000, v30
	v_mul_f32_e32 v14, v31, v31
	v_mul_f32_e32 v15, v33, v33
	v_fmac_f32_e32 v14, v30, v30
	v_fmac_f32_e32 v15, v32, v32
	v_add_f32_e32 v14, v14, v15
	v_fmac_f32_e32 v49, 0xba000000, v12
	v_fmac_f32_e32 v29, 0xba000000, v12
	v_add_f32_e32 v13, v14, v13
	v_fmamk_f32 v48, v12, 0xba000000, v48
	v_fmamk_f32 v28, v12, 0xba000000, v28
	v_mul_f32_e32 v14, v29, v29
	v_mul_f32_e32 v15, v49, v49
	v_fmac_f32_e32 v14, v28, v28
	v_fmac_f32_e32 v15, v48, v48
	v_add_f32_e32 v14, v14, v15
	v_fmac_f32_e32 v53, 0xba000000, v12
	v_fmac_f32_e32 v51, 0xba000000, v12
	v_add_f32_e32 v13, v14, v13
	v_fmamk_f32 v52, v12, 0xba000000, v52
	v_fmamk_f32 v50, v12, 0xba000000, v50
	v_mul_f32_e32 v14, v51, v51
	v_mul_f32_e32 v15, v53, v53
	v_fmac_f32_e32 v14, v50, v50
	v_fmac_f32_e32 v15, v52, v52
	v_add_f32_e32 v14, v14, v15
	v_fmac_f32_e32 v25, 0xba000000, v12
	v_fmac_f32_e32 v21, 0xba000000, v12
	v_add_f32_e32 v13, v14, v13
	v_fmamk_f32 v24, v12, 0xba000000, v24
	v_fmamk_f32 v20, v12, 0xba000000, v20
	v_mul_f32_e32 v14, v21, v21
	v_mul_f32_e32 v15, v25, v25
	v_fmac_f32_e32 v14, v20, v20
	v_fmac_f32_e32 v15, v24, v24
	v_add_f32_e32 v14, v14, v15
	v_fmac_f32_e32 v5, 0xba000000, v12
	v_fmac_f32_e32 v3, 0xba000000, v12
	v_add_f32_e32 v13, v14, v13
	v_fmamk_f32 v4, v12, 0xba000000, v4
	v_fmamk_f32 v2, v12, 0xba000000, v2
	v_mul_f32_e32 v14, v3, v3
	v_mul_f32_e32 v15, v5, v5
	v_fmac_f32_e32 v14, v2, v2
	v_fmac_f32_e32 v15, v4, v4
	v_add_f32_e32 v14, v14, v15
	v_fmac_f32_e32 v7, 0xba000000, v12
	v_fmac_f32_e32 v9, 0xba000000, v12
	v_add_f32_e32 v13, v14, v13
	v_fmamk_f32 v6, v12, 0xba000000, v6
	v_fmamk_f32 v8, v12, 0xba000000, v8
	v_mul_f32_e32 v12, v9, v9
	v_mul_f32_e32 v14, v7, v7
	v_fmac_f32_e32 v12, v8, v8
	v_fmac_f32_e32 v14, v6, v6
	v_add_f32_e32 v12, v12, v14
	v_add_f32_e32 v17, v12, v13
	v_lshlrev_b64 v[12:13], 13, v[46:47]
	v_lshl_add_u64 v[14:15], s[26:27], 0, v[12:13]
	s_nop 0
	v_add_f32_dpp v12, v17, v17 quad_perm:[1,0,3,2] row_mask:0xf bank_mask:0xf bound_ctrl:1
	s_nop 1
	v_add_f32_dpp v12, v12, v12 quad_perm:[2,3,0,1] row_mask:0xf bank_mask:0xf bound_ctrl:1
	s_nop 1
	v_add_f32_dpp v12, v12, v12 row_half_mirror row_mask:0xf bank_mask:0xf bound_ctrl:1
	s_nop 1
	v_add_f32_dpp v12, v12, v12 row_mirror row_mask:0xf bank_mask:0xf bound_ctrl:1
	v_mov_b32_e32 v13, v12
	s_nop 1
	v_permlane16_swap_b32_e32 v12, v13
	v_add_f32_e32 v12, v12, v13
	v_mov_b32_e32 v13, v12
	s_nop 1
	v_permlane32_swap_b32_e32 v12, v13
	v_add_f32_e32 v12, v12, v13
	v_fmamk_f32 v12, v12, 0x3a000000, v212
	v_cmp_gt_f32_e32 vcc, s8, v12
	v_mul_f32_e32 v13, 0x4b800000, v12
	s_movk_i32 s8, 0x3fff
	v_cndmask_b32_e32 v12, v12, v13, vcc
	v_rsq_f32_e32 v12, v12
	s_nop 0
	v_mul_f32_e32 v13, 0x45800000, v12
	v_cndmask_b32_e32 v12, v12, v13, vcc
	v_pk_mul_f32 v[18:19], v[44:45], v[12:13] op_sel_hi:[1,0]
	v_pk_mul_f32 v[40:41], v[40:41], v[12:13] op_sel_hi:[1,0]
	v_add_u32_e32 v13, 0, v56
	ds_read_b128 v[44:47], v13 offset:16384
	ds_read_b128 v[56:59], v13 offset:24576
	v_cmp_lt_i32_e32 vcc, s8, v10
	s_or_b64 s[2:3], vcc, s[2:3]
	s_waitcnt lgkmcnt(0)
	v_pk_fma_f32 v[46:47], v[46:47], v[40:41], v[58:59]
	v_pk_fma_f32 v[44:45], v[44:45], v[18:19], v[56:57]
	v_lshl_add_u64 v[18:19], v[42:43], 2, v[14:15]
	global_store_dwordx4 v[18:19], v[44:47], off
	v_pk_mul_f32 v[18:19], v[36:37], v[12:13] op_sel_hi:[1,0]
	s_nop 0
	v_pk_mul_f32 v[44:45], v[34:35], v[12:13] op_sel_hi:[1,0]
	ds_read_b128 v[34:37], v13 offset:16400
	ds_read_b128 v[40:43], v13 offset:24592
	s_waitcnt lgkmcnt(0)
	v_pk_fma_f32 v[34:35], v[34:35], v[44:45], v[40:41]
	v_pk_fma_f32 v[36:37], v[36:37], v[18:19], v[42:43]
	v_lshl_add_u64 v[18:19], v[38:39], 2, v[14:15]
	global_store_dwordx4 v[18:19], v[34:37], off offset:16
	v_pk_mul_f32 v[38:39], v[32:33], v[12:13] op_sel_hi:[1,0]
	v_pk_mul_f32 v[40:41], v[30:31], v[12:13] op_sel_hi:[1,0]
	ds_read_b128 v[30:33], v13 offset:16896
	ds_read_b128 v[34:37], v13 offset:25088
	s_waitcnt lgkmcnt(0)
	v_pk_fma_f32 v[30:31], v[30:31], v[40:41], v[34:35]
	v_pk_fma_f32 v[32:33], v[32:33], v[38:39], v[36:37]
	global_store_dwordx4 v[18:19], v[30:33], off offset:512
	v_pk_mul_f32 v[38:39], v[28:29], v[12:13] op_sel_hi:[1,0]
	ds_read_b128 v[28:31], v13 offset:16912
	ds_read_b128 v[32:35], v13 offset:25104
	v_pk_mul_f32 v[36:37], v[48:49], v[12:13] op_sel_hi:[1,0]
	s_waitcnt lgkmcnt(0)
	v_pk_fma_f32 v[28:29], v[28:29], v[38:39], v[32:33]
	v_pk_fma_f32 v[30:31], v[30:31], v[36:37], v[34:35]
	global_store_dwordx4 v[18:19], v[28:31], off offset:528
	ds_read_b128 v[28:31], v13 offset:20480
	ds_read_b128 v[32:35], v13 offset:28672
	v_pk_mul_f32 v[18:19], v[52:53], v[12:13] op_sel_hi:[1,0]
	v_pk_mul_f32 v[36:37], v[50:51], v[12:13] op_sel_hi:[1,0]
	s_waitcnt lgkmcnt(0)
	v_pk_fma_f32 v[30:31], v[18:19], v[30:31], v[34:35]
	v_pk_fma_f32 v[28:29], v[36:37], v[28:29], v[32:33]
	v_lshl_add_u64 v[18:19], v[26:27], 2, v[14:15]
	global_store_dwordx4 v[18:19], v[28:31], off
	v_lshl_add_u64 v[14:15], v[22:23], 2, v[14:15]
	v_pk_mul_f32 v[22:23], v[4:5], v[12:13] op_sel_hi:[1,0]
	v_pk_mul_f32 v[28:29], v[24:25], v[12:13] op_sel_hi:[1,0]
	v_pk_mul_f32 v[30:31], v[20:21], v[12:13] op_sel_hi:[1,0]
	ds_read_b128 v[18:21], v11 offset:20480
	ds_read_b128 v[24:27], v11 offset:28672
	v_add_u32_e32 v11, 0, v55
	s_waitcnt lgkmcnt(0)
	v_pk_fma_f32 v[18:19], v[30:31], v[18:19], v[24:25]
	v_pk_fma_f32 v[20:21], v[28:29], v[20:21], v[26:27]
	global_store_dwordx4 v[14:15], v[18:21], off offset:16
	v_pk_mul_f32 v[24:25], v[2:3], v[12:13] op_sel_hi:[1,0]
	ds_read_b128 v[2:5], v11 offset:20480
	ds_read_b128 v[18:21], v11 offset:28672
	s_waitcnt lgkmcnt(0)
	v_pk_fma_f32 v[2:3], v[24:25], v[2:3], v[18:19]
	v_pk_fma_f32 v[4:5], v[22:23], v[4:5], v[20:21]
	global_store_dwordx4 v[14:15], v[2:5], off offset:512
	v_pk_mul_f32 v[18:19], v[6:7], v[12:13] op_sel_hi:[1,0]
	v_add_u32_e32 v6, 0, v16
	v_pk_mul_f32 v[12:13], v[8:9], v[12:13] op_sel_hi:[1,0]
	ds_read_b128 v[2:5], v6 offset:20480
	ds_read_b128 v[6:9], v6 offset:28672
	s_waitcnt lgkmcnt(0)
	v_pk_fma_f32 v[2:3], v[12:13], v[2:3], v[6:7]
	v_pk_fma_f32 v[4:5], v[18:19], v[4:5], v[8:9]
	global_store_dwordx4 v[14:15], v[2:5], off offset:528
	s_andn2_b64 exec, exec, s[2:3]
	s_cbranch_execnz .LBB0_3777
	s_branch .LBB0_3758
